# baseline (speedup 1.0000x reference)
_Z11attn_kernelPK14__hip_bfloat16S1_S1_PS_:
	s_lshr_b32 s3, s2, 3
	s_and_b32 s33, s2, 7
	s_sub_i32 s4, 63, s3
	s_sub_i32 s3, s3, 32
	s_cmpk_lt_u32 s2, 0x100
	s_cselect_b32 s2, s4, s3
	v_lshrrev_b32_e32 v1, 6, v0
	s_ashr_i32 s77, s2, 1
	v_and_b32_e32 v184, 63, v0
	v_bfe_u32 v186, v0, 5, 1
	v_and_b32_e32 v185, 31, v0
	s_lshl_b32 s76, s2, 5
	v_cmp_ge_i32_e32 vcc, s77, v1
	v_mbcnt_lo_u32_b32 v50, -1, 0
	s_and_saveexec_b64 s[4:5], vcc
	s_xor_b64 s[70:71], exec, s[4:5]
	s_cbranch_execz .LBB2_8
	s_load_dwordx4 s[4:7], s[0:1], 0x0
	s_load_dwordx2 s[8:9], s[0:1], 0x10
	s_lshl_b32 s3, s33, 8
	s_lshl_b32 s2, s2, 2
	s_add_i32 s2, s2, s3
	s_ashr_i32 s3, s2, 31
	s_lshl_b64 s[2:3], s[2:3], 10
	s_waitcnt lgkmcnt(0)
	s_add_u32 s2, s4, s2
	s_addc_u32 s3, s5, s3
	s_lshl_b32 s10, s33, 18
	s_add_u32 s4, s6, s10
	s_addc_u32 s5, s7, 0
	s_add_u32 s6, s8, s10
	v_lshlrev_b32_e32 v34, 4, v184
	v_mov_b32_e32 v35, 0
	s_addc_u32 s7, s9, 0
	s_mov_b64 s[80:81], s[4:5]
	s_mov_b64 s[82:83], s[6:7]
	v_lshlrev_b32_e32 v203, 4, v184
	v_readfirstlane_b32 s78, v1
	global_load_dwordx4 v[68:71], v34, s[2:3]
	global_load_dwordx4 v[72:75], v34, s[2:3] offset:1024
	global_load_dwordx4 v[76:79], v34, s[2:3] offset:2048
	global_load_dwordx4 v[80:83], v34, s[2:3] offset:3072
	v_lshl_add_u64 v[180:181], s[4:5], 0, v[34:35]
	v_lshl_add_u64 v[182:183], s[6:7], 0, v[34:35]
	v_lshlrev_b32_e32 v34, 13, v1
	v_lshl_add_u64 v[2:3], v[180:181], 0, v[34:35]
	global_load_dwordx4 v[100:103], v[2:3], off nt
	global_load_dwordx4 v[108:111], v[2:3], off offset:1024 nt
	global_load_dwordx4 v[116:119], v[2:3], off offset:2048 nt
	global_load_dwordx4 v[120:123], v[2:3], off offset:3072 nt
	v_or_b32_e32 v2, 0x1000, v34
	v_mov_b32_e32 v3, v35
	v_lshl_add_u64 v[4:5], v[180:181], 0, v[2:3]
	v_or_b32_e32 v6, 0x1400, v34
	v_mov_b32_e32 v7, v35
	v_lshl_add_u64 v[8:9], v[180:181], 0, v[6:7]
	global_load_dwordx4 v[132:135], v[4:5], off nt
	global_load_dwordx4 v[136:139], v[8:9], off nt
	v_or_b32_e32 v4, 0x1800, v34
	v_mov_b32_e32 v5, v35
	v_lshl_add_u64 v[8:9], v[180:181], 0, v[4:5]
	v_or_b32_e32 v10, 0x1c00, v34
	v_mov_b32_e32 v11, v35
	v_lshl_add_u64 v[12:13], v[180:181], 0, v[10:11]
	global_load_dwordx4 v[140:143], v[8:9], off nt
	global_load_dwordx4 v[144:147], v[12:13], off nt
	v_lshl_add_u64 v[8:9], v[182:183], 0, v[34:35]
	global_load_dwordx4 v[128:131], v[8:9], off nt
	global_load_dwordx4 v[124:127], v[8:9], off offset:1024 nt
	global_load_dwordx4 v[112:115], v[8:9], off offset:2048 nt
	global_load_dwordx4 v[104:107], v[8:9], off offset:3072 nt
	v_lshl_add_u64 v[2:3], v[182:183], 0, v[2:3]
	v_lshl_add_u64 v[6:7], v[182:183], 0, v[6:7]
	global_load_dwordx4 v[84:87], v[2:3], off nt
	global_load_dwordx4 v[96:99], v[6:7], off nt
	v_lshl_add_u64 v[2:3], v[182:183], 0, v[4:5]
	v_lshl_add_u64 v[4:5], v[182:183], 0, v[10:11]
	global_load_dwordx4 v[88:91], v[2:3], off nt
	global_load_dwordx4 v[92:95], v[4:5], off nt
	v_lshlrev_b32_e32 v2, 2, v186
	v_lshl_or_b32 v2, s77, 6, v2
	v_or_b32_e32 v14, s76, v185
	v_or_b32_e32 v3, 32, v2
	v_cmp_gt_i32_e64 s[4:5], v3, v14
	v_or_b32_e32 v3, 33, v2
	v_cmp_gt_i32_e64 s[8:9], v3, v14
	v_or_b32_e32 v3, 2, v2
	v_cmp_gt_i32_e64 s[10:11], v3, v14
	v_or_b32_e32 v3, 34, v2
	v_cmp_gt_i32_e64 s[12:13], v3, v14
	v_or_b32_e32 v3, 3, v2
	v_cmp_gt_i32_e64 s[14:15], v3, v14
	v_or_b32_e32 v3, 35, v2
	v_cmp_gt_i32_e64 s[16:17], v3, v14
	v_or_b32_e32 v3, 8, v2
	v_cmp_gt_i32_e64 s[18:19], v3, v14
	v_or_b32_e32 v3, 40, v2
	v_cmp_gt_i32_e64 s[20:21], v3, v14
	v_or_b32_e32 v3, 9, v2
	v_cmp_gt_i32_e64 s[22:23], v3, v14
	v_or_b32_e32 v3, 41, v2
	v_cmp_gt_i32_e64 s[24:25], v3, v14
	v_or_b32_e32 v3, 10, v2
	v_cmp_gt_i32_e64 s[26:27], v3, v14
	v_or_b32_e32 v3, 42, v2
	v_cmp_gt_i32_e64 s[28:29], v3, v14
	v_or_b32_e32 v3, 11, v2
	v_cmp_gt_i32_e64 s[30:31], v3, v14
	v_or_b32_e32 v3, 43, v2
	v_cmp_gt_i32_e64 s[34:35], v3, v14
	v_or_b32_e32 v3, 16, v2
	v_cmp_gt_i32_e64 s[36:37], v3, v14
	v_or_b32_e32 v3, 48, v2
	v_cmp_gt_i32_e64 s[38:39], v3, v14
	v_or_b32_e32 v3, 17, v2
	v_cmp_gt_i32_e64 s[40:41], v3, v14
	v_or_b32_e32 v3, 49, v2
	v_cmp_gt_i32_e64 s[42:43], v3, v14
	v_or_b32_e32 v3, 18, v2
	v_cmp_gt_i32_e64 s[44:45], v3, v14
	v_or_b32_e32 v3, 50, v2
	v_cmp_gt_i32_e64 s[46:47], v3, v14
	v_or_b32_e32 v3, 19, v2
	v_cmp_gt_i32_e64 s[48:49], v3, v14
	v_or_b32_e32 v3, 51, v2
	v_cmp_gt_i32_e64 s[50:51], v3, v14
	v_or_b32_e32 v3, 24, v2
	v_cmp_gt_i32_e64 s[52:53], v3, v14
	v_or_b32_e32 v3, 56, v2
	v_cmp_gt_i32_e64 s[54:55], v3, v14
	v_or_b32_e32 v3, 25, v2
	v_cmp_gt_i32_e64 s[56:57], v3, v14
	v_or_b32_e32 v3, 57, v2
	v_cmp_gt_i32_e64 s[58:59], v3, v14
	v_or_b32_e32 v3, 26, v2
	v_cmp_gt_i32_e64 s[60:61], v3, v14
	v_or_b32_e32 v3, 58, v2
	v_cmp_gt_i32_e64 s[2:3], v2, v14
	v_cmp_lt_i32_e64 s[6:7], v2, v14
	v_cmp_gt_i32_e64 s[62:63], v3, v14
	v_or_b32_e32 v3, 27, v2
	v_or_b32_e32 v2, 59, v2
	v_mov_b32_e32 v34, v35
	v_cmp_gt_i32_e64 s[64:65], v3, v14
	v_cmp_gt_i32_e64 s[66:67], v2, v14
	v_mov_b32_e32 v36, v35
	v_mov_b32_e32 v37, v35
	v_mov_b32_e32 v38, v35
	v_mov_b32_e32 v39, v35
	v_mov_b32_e32 v40, v35
	v_mov_b32_e32 v41, v35
	v_mov_b32_e32 v42, v35
	v_mov_b32_e32 v43, v35
	v_mov_b32_e32 v44, v35
	v_mov_b32_e32 v45, v35
	v_mov_b32_e32 v46, v35
	v_mov_b32_e32 v47, v35
	v_mov_b32_e32 v48, v35
	v_mov_b32_e32 v49, v35
	v_mov_b64_e32 v[18:19], v[34:35]
	v_mov_b64_e32 v[2:3], v[34:35]
	v_mov_b32_e32 v190, 0xf149f2ca
	s_mov_b64 s[72:73], 0
	v_mbcnt_hi_u32_b32 v188, -1, v50
	v_mov_b32_e32 v187, 0
	v_mov_b64_e32 v[20:21], v[36:37]
	v_mov_b64_e32 v[22:23], v[38:39]
	v_mov_b64_e32 v[24:25], v[40:41]
	v_mov_b64_e32 v[26:27], v[42:43]
	v_mov_b64_e32 v[28:29], v[44:45]
	v_mov_b64_e32 v[30:31], v[46:47]
	v_mov_b64_e32 v[32:33], v[48:49]
	v_mov_b32_e32 v189, 0xf149f2ca
	v_mov_b32_e32 v191, v1
	v_mov_b64_e32 v[4:5], v[36:37]
	v_mov_b64_e32 v[6:7], v[38:39]
	v_mov_b64_e32 v[8:9], v[40:41]
	v_mov_b64_e32 v[10:11], v[42:43]
	v_mov_b64_e32 v[12:13], v[44:45]
	v_mov_b64_e32 v[14:15], v[46:47]
	v_mov_b64_e32 v[16:17], v[48:49]
	s_branch .LBB2_3
